# out-proj GEMM epilogue de-serialised: the 16 residual-row reads of a tile are touched up front (one round trip) so the compiler's load-wait-store ladder hits cache
# speedup vs baseline: 1.0070x; 1.0021x over previous
.LBB0_1039:
	s_add_u32 s4, s36, 0xfff80080
	s_addc_u32 s5, s37, -1
	s_add_i32 s64, 0, 0x10000
	v_add_u32_e32 v142, s64, v179
	ds_read_b128 v[130:133], v142
	ds_read_b128 v[134:137], v142 offset:1024
	ds_read_b128 v[138:141], v142 offset:2048
	ds_read_b128 v[142:145], v142 offset:3072
	s_cmp_eq_u32 s92, 28
	s_cselect_b32 s55, s49, s5
	s_cselect_b32 s54, s89, s4
	s_cselect_b32 s5, s47, s24
	s_cselect_b32 s4, s14, s10
	v_lshl_add_u64 v[160:161], s[36:37], 0, v[152:153]
	s_add_i32 m0, s20, 0xc000
	ds_read_b128 v[156:159], v181
	ds_read_b128 v[174:177], v181 offset:1024
	ds_read_b128 v[182:185], v181 offset:2048
	ds_read_b128 v[186:189], v181 offset:3072
	ds_read_b128 v[190:193], v181 offset:4096
	ds_read_b128 v[194:197], v181 offset:5120
	ds_read_b128 v[198:201], v181 offset:6144
	ds_read_b128 v[206:209], v181 offset:7168
	global_load_lds_dwordx4 v[160:161], off
	v_lshl_add_u64 v[160:161], s[36:37], 0, v[154:155]
	s_add_i32 m0, s20, 0xe000
	s_nop 0
	global_load_lds_dwordx4 v[160:161], off
	s_waitcnt lgkmcnt(8)
	s_barrier
	s_waitcnt lgkmcnt(0)
	s_setprio 1
	s_waitcnt lgkmcnt(0)
	v_mfma_f32_16x16x32_bf16 v[126:129], v[130:133], v[156:159], v[126:129]
	v_mfma_f32_16x16x32_bf16 v[122:125], v[138:141], v[156:159], v[122:125]
	v_mfma_f32_16x16x32_bf16 v[110:113], v[130:133], v[182:185], v[110:113]
	v_mfma_f32_16x16x32_bf16 v[106:109], v[138:141], v[182:185], v[106:109]
	v_mfma_f32_16x16x32_bf16 v[92:95], v[130:133], v[190:193], v[92:95]
	v_mfma_f32_16x16x32_bf16 v[88:91], v[138:141], v[190:193], v[88:91]
	v_mfma_f32_16x16x32_bf16 v[76:79], v[130:133], v[198:201], v[76:79]
	v_mfma_f32_16x16x32_bf16 v[72:75], v[138:141], v[198:201], v[72:75]
	v_mfma_f32_16x16x32_bf16 v[126:129], v[134:137], v[174:177], v[126:129]
	v_mfma_f32_16x16x32_bf16 v[122:125], v[142:145], v[174:177], v[122:125]
	v_mfma_f32_16x16x32_bf16 v[110:113], v[134:137], v[186:189], v[110:113]
	v_mfma_f32_16x16x32_bf16 v[106:109], v[142:145], v[186:189], v[106:109]
	v_mfma_f32_16x16x32_bf16 v[92:95], v[134:137], v[194:197], v[92:95]
	v_mfma_f32_16x16x32_bf16 v[88:91], v[142:145], v[194:197], v[88:91]
	v_mfma_f32_16x16x32_bf16 v[76:79], v[134:137], v[206:209], v[76:79]
	v_mfma_f32_16x16x32_bf16 v[72:75], v[142:145], v[206:209], v[72:75]
	s_setprio 0
	s_barrier
	s_add_i32 s66, 0, 0x14000
	v_add_u32_e32 v160, s66, v179
	s_add_i32 s64, s64, s8
	ds_read_b128 v[228:231], v160
	ds_read_b128 v[232:235], v160 offset:1024
	ds_read_b128 v[236:239], v160 offset:2048
	ds_read_b128 v[240:243], v160 offset:3072
	v_lshl_add_u64 v[160:161], s[4:5], 0, v[96:97]
	s_mov_b32 m0, s64
	v_lshl_add_u64 v[202:203], s[4:5], 0, v[146:147]
	global_load_lds_dwordx4 v[160:161], off
	s_add_i32 m0, s64, 0x2000
	s_nop 0
	global_load_lds_dwordx4 v[202:203], off
	s_barrier
	s_waitcnt lgkmcnt(0)
	s_setprio 1
	s_waitcnt lgkmcnt(0)
	v_mfma_f32_16x16x32_bf16 v[118:121], v[228:231], v[156:159], v[118:121]
	v_mfma_f32_16x16x32_bf16 v[114:117], v[236:239], v[156:159], v[114:117]
	v_mfma_f32_16x16x32_bf16 v[102:105], v[228:231], v[182:185], v[102:105]
	v_mfma_f32_16x16x32_bf16 v[98:101], v[236:239], v[182:185], v[98:101]
	v_mfma_f32_16x16x32_bf16 v[84:87], v[228:231], v[190:193], v[84:87]
	v_mfma_f32_16x16x32_bf16 v[80:83], v[236:239], v[190:193], v[80:83]
	v_mfma_f32_16x16x32_bf16 v[68:71], v[228:231], v[198:201], v[68:71]
	v_mfma_f32_16x16x32_bf16 v[64:67], v[236:239], v[198:201], v[64:67]
	v_mfma_f32_16x16x32_bf16 v[118:121], v[232:235], v[174:177], v[118:121]
	v_mfma_f32_16x16x32_bf16 v[114:117], v[240:243], v[174:177], v[114:117]
	v_mfma_f32_16x16x32_bf16 v[102:105], v[232:235], v[186:189], v[102:105]
	v_mfma_f32_16x16x32_bf16 v[98:101], v[240:243], v[186:189], v[98:101]
	v_mfma_f32_16x16x32_bf16 v[84:87], v[232:235], v[194:197], v[84:87]
	v_mfma_f32_16x16x32_bf16 v[80:83], v[240:243], v[194:197], v[80:83]
	v_mfma_f32_16x16x32_bf16 v[68:71], v[232:235], v[206:209], v[68:71]
	v_mfma_f32_16x16x32_bf16 v[64:67], v[240:243], v[206:209], v[64:67]
	s_setprio 0
	s_mov_b32 m0, s20
	v_lshl_add_u64 v[212:213], s[54:55], 0, v[150:151]
	s_barrier
	ds_read_b128 v[156:159], v181 offset:16384
	ds_read_b128 v[174:177], v181 offset:17408
	ds_read_b128 v[182:185], v181 offset:18432
	ds_read_b128 v[186:189], v181 offset:19456
	ds_read_b128 v[190:193], v181 offset:20480
	ds_read_b128 v[194:197], v181 offset:21504
	ds_read_b128 v[198:201], v181 offset:22528
	ds_read_b128 v[206:209], v181 offset:23552
	global_load_lds_dwordx4 v[212:213], off
	v_lshl_add_u64 v[244:245], s[54:55], 0, v[148:149]
	s_mov_b32 m0, s21
	s_nop 0
	global_load_lds_dwordx4 v[244:245], off
	s_barrier
	s_waitcnt lgkmcnt(0)
	s_setprio 1
	s_waitcnt lgkmcnt(0)
	v_mfma_f32_16x16x32_bf16 v[60:63], v[130:133], v[156:159], v[60:63]
	v_mfma_f32_16x16x32_bf16 v[56:59], v[138:141], v[156:159], v[56:59]
	v_mfma_f32_16x16x32_bf16 v[44:47], v[130:133], v[182:185], v[44:47]
	v_mfma_f32_16x16x32_bf16 v[40:43], v[138:141], v[182:185], v[40:43]
	v_mfma_f32_16x16x32_bf16 v[28:31], v[130:133], v[190:193], v[28:31]
	v_mfma_f32_16x16x32_bf16 v[24:27], v[138:141], v[190:193], v[24:27]
	v_mfma_f32_16x16x32_bf16 v[12:15], v[130:133], v[198:201], v[12:15]
	v_mfma_f32_16x16x32_bf16 v[8:11], v[138:141], v[198:201], v[8:11]
	v_mfma_f32_16x16x32_bf16 v[60:63], v[134:137], v[174:177], v[60:63]
	v_mfma_f32_16x16x32_bf16 v[56:59], v[142:145], v[174:177], v[56:59]
	v_mfma_f32_16x16x32_bf16 v[44:47], v[134:137], v[186:189], v[44:47]
	v_mfma_f32_16x16x32_bf16 v[40:43], v[142:145], v[186:189], v[40:43]
	v_mfma_f32_16x16x32_bf16 v[28:31], v[134:137], v[194:197], v[28:31]
	v_mfma_f32_16x16x32_bf16 v[24:27], v[142:145], v[194:197], v[24:27]
	v_mfma_f32_16x16x32_bf16 v[12:15], v[134:137], v[206:209], v[12:15]
	v_mfma_f32_16x16x32_bf16 v[8:11], v[142:145], v[206:209], v[8:11]
	s_setprio 0
	s_barrier
	s_add_u32 s64, s4, 0x80000
	s_addc_u32 s65, s5, 0
	s_add_i32 s66, s66, s8
	v_lshl_add_u64 v[130:131], s[64:65], 0, v[96:97]
	s_mov_b32 m0, s66
	s_nop 0
	global_load_lds_dwordx4 v[130:131], off
	v_lshl_add_u64 v[130:131], s[64:65], 0, v[146:147]
	s_add_i32 m0, s66, 0x2000
	s_nop 0
	global_load_lds_dwordx4 v[130:131], off
	s_waitcnt vmcnt(6)
	s_barrier
	s_setprio 1
	v_mfma_f32_16x16x32_bf16 v[52:55], v[228:231], v[156:159], v[52:55]
	v_mfma_f32_16x16x32_bf16 v[48:51], v[236:239], v[156:159], v[48:51]
	v_mfma_f32_16x16x32_bf16 v[36:39], v[228:231], v[182:185], v[36:39]
	v_mfma_f32_16x16x32_bf16 v[32:35], v[236:239], v[182:185], v[32:35]
	v_mfma_f32_16x16x32_bf16 v[20:23], v[228:231], v[190:193], v[20:23]
	v_mfma_f32_16x16x32_bf16 v[16:19], v[236:239], v[190:193], v[16:19]
	v_mfma_f32_16x16x32_bf16 v[4:7], v[228:231], v[198:201], v[4:7]
	v_mfma_f32_16x16x32_bf16 v[0:3], v[236:239], v[198:201], v[0:3]
	v_mfma_f32_16x16x32_bf16 v[52:55], v[232:235], v[174:177], v[52:55]
	v_mfma_f32_16x16x32_bf16 v[48:51], v[240:243], v[174:177], v[48:51]
	v_mfma_f32_16x16x32_bf16 v[36:39], v[232:235], v[186:189], v[36:39]
	v_mfma_f32_16x16x32_bf16 v[32:35], v[240:243], v[186:189], v[32:35]
	v_mfma_f32_16x16x32_bf16 v[20:23], v[232:235], v[194:197], v[20:23]
	v_mfma_f32_16x16x32_bf16 v[16:19], v[240:243], v[194:197], v[16:19]
	v_mfma_f32_16x16x32_bf16 v[4:7], v[232:235], v[206:209], v[4:7]
	v_mfma_f32_16x16x32_bf16 v[0:3], v[240:243], v[206:209], v[0:3]
	s_setprio 0
	s_add_i32 s64, 0, 0x18000
	v_add_u32_e32 v142, s64, v179
	s_barrier
	ds_read_b128 v[130:133], v142
	ds_read_b128 v[134:137], v142 offset:1024
	ds_read_b128 v[138:141], v142 offset:2048
	ds_read_b128 v[142:145], v142 offset:3072
	s_add_u32 s54, s54, 0x80000
	s_addc_u32 s55, s55, 0
	s_mov_b32 m0, s38
	v_lshl_add_u64 v[228:229], s[54:55], 0, v[150:151]
	ds_read_b128 v[156:159], v181 offset:32768
	ds_read_b128 v[174:177], v181 offset:33792
	ds_read_b128 v[182:185], v181 offset:34816
	ds_read_b128 v[186:189], v181 offset:35840
	ds_read_b128 v[190:193], v181 offset:36864
	ds_read_b128 v[194:197], v181 offset:37888
	ds_read_b128 v[198:201], v181 offset:38912
	ds_read_b128 v[206:209], v181 offset:39936
	global_load_lds_dwordx4 v[228:229], off
	v_lshl_add_u64 v[228:229], s[54:55], 0, v[148:149]
	s_mov_b32 m0, s39
	s_nop 0
	global_load_lds_dwordx4 v[228:229], off
	s_waitcnt lgkmcnt(8)
	s_barrier
	s_waitcnt lgkmcnt(0)
	s_setprio 1
	s_waitcnt lgkmcnt(0)
	v_mfma_f32_16x16x32_bf16 v[126:129], v[130:133], v[156:159], v[126:129]
	v_mfma_f32_16x16x32_bf16 v[122:125], v[138:141], v[156:159], v[122:125]
	v_mfma_f32_16x16x32_bf16 v[110:113], v[130:133], v[182:185], v[110:113]
	v_mfma_f32_16x16x32_bf16 v[106:109], v[138:141], v[182:185], v[106:109]
	v_mfma_f32_16x16x32_bf16 v[92:95], v[130:133], v[190:193], v[92:95]
	v_mfma_f32_16x16x32_bf16 v[88:91], v[138:141], v[190:193], v[88:91]
	v_mfma_f32_16x16x32_bf16 v[76:79], v[130:133], v[198:201], v[76:79]
	v_mfma_f32_16x16x32_bf16 v[72:75], v[138:141], v[198:201], v[72:75]
	v_mfma_f32_16x16x32_bf16 v[126:129], v[134:137], v[174:177], v[126:129]
	v_mfma_f32_16x16x32_bf16 v[122:125], v[142:145], v[174:177], v[122:125]
	v_mfma_f32_16x16x32_bf16 v[110:113], v[134:137], v[186:189], v[110:113]
	v_mfma_f32_16x16x32_bf16 v[106:109], v[142:145], v[186:189], v[106:109]
	v_mfma_f32_16x16x32_bf16 v[92:95], v[134:137], v[194:197], v[92:95]
	v_mfma_f32_16x16x32_bf16 v[88:91], v[142:145], v[194:197], v[88:91]
	v_mfma_f32_16x16x32_bf16 v[76:79], v[134:137], v[206:209], v[76:79]
	v_mfma_f32_16x16x32_bf16 v[72:75], v[142:145], v[206:209], v[72:75]
	s_setprio 0
	s_barrier
	s_add_i32 s54, 0, 0x1c000
	s_add_i32 s55, s64, s8
	v_add_u32_e32 v204, s54, v179
	v_lshl_add_u64 v[160:161], v[160:161], 0, s[18:19]
	s_mov_b32 m0, s55
	ds_read_b128 v[228:231], v204
	ds_read_b128 v[232:235], v204 offset:1024
	ds_read_b128 v[236:239], v204 offset:2048
	ds_read_b128 v[240:243], v204 offset:3072
	global_load_lds_dwordx4 v[160:161], off
	v_lshl_add_u64 v[160:161], v[202:203], 0, s[18:19]
	s_add_i32 m0, s55, 0x2000
	s_nop 0
	global_load_lds_dwordx4 v[160:161], off
	s_barrier
	s_waitcnt lgkmcnt(0)
	s_setprio 1
	s_waitcnt lgkmcnt(0)
	v_mfma_f32_16x16x32_bf16 v[118:121], v[228:231], v[156:159], v[118:121]
	v_mfma_f32_16x16x32_bf16 v[114:117], v[236:239], v[156:159], v[114:117]
	v_mfma_f32_16x16x32_bf16 v[102:105], v[228:231], v[182:185], v[102:105]
	v_mfma_f32_16x16x32_bf16 v[98:101], v[236:239], v[182:185], v[98:101]
	v_mfma_f32_16x16x32_bf16 v[84:87], v[228:231], v[190:193], v[84:87]
	v_mfma_f32_16x16x32_bf16 v[80:83], v[236:239], v[190:193], v[80:83]
	v_mfma_f32_16x16x32_bf16 v[68:71], v[228:231], v[198:201], v[68:71]
	v_mfma_f32_16x16x32_bf16 v[64:67], v[236:239], v[198:201], v[64:67]
	v_mfma_f32_16x16x32_bf16 v[118:121], v[232:235], v[174:177], v[118:121]
	v_mfma_f32_16x16x32_bf16 v[114:117], v[240:243], v[174:177], v[114:117]
	v_mfma_f32_16x16x32_bf16 v[102:105], v[232:235], v[186:189], v[102:105]
	v_mfma_f32_16x16x32_bf16 v[98:101], v[240:243], v[186:189], v[98:101]
	v_mfma_f32_16x16x32_bf16 v[84:87], v[232:235], v[194:197], v[84:87]
	v_mfma_f32_16x16x32_bf16 v[80:83], v[240:243], v[194:197], v[80:83]
	v_mfma_f32_16x16x32_bf16 v[68:71], v[232:235], v[206:209], v[68:71]
	v_mfma_f32_16x16x32_bf16 v[64:67], v[240:243], v[206:209], v[64:67]
	s_setprio 0
	s_mov_b32 m0, s74
	v_lshl_add_u64 v[160:161], v[212:213], 0, s[18:19]
	s_barrier
	ds_read_b128 v[156:159], v181 offset:49152
	ds_read_b128 v[174:177], v181 offset:50176
	ds_read_b128 v[182:185], v181 offset:51200
	ds_read_b128 v[186:189], v181 offset:52224
	ds_read_b128 v[190:193], v181 offset:53248
	ds_read_b128 v[194:197], v181 offset:54272
	ds_read_b128 v[198:201], v181 offset:55296
	ds_read_b128 v[206:209], v181 offset:56320
	global_load_lds_dwordx4 v[160:161], off
	v_lshl_add_u64 v[160:161], v[244:245], 0, s[18:19]
	s_mov_b32 m0, s79
	s_nop 0
	global_load_lds_dwordx4 v[160:161], off
	s_barrier
	s_waitcnt lgkmcnt(0)
	s_setprio 1
	s_waitcnt lgkmcnt(0)
	v_mfma_f32_16x16x32_bf16 v[60:63], v[130:133], v[156:159], v[60:63]
	v_mfma_f32_16x16x32_bf16 v[56:59], v[138:141], v[156:159], v[56:59]
	v_mfma_f32_16x16x32_bf16 v[44:47], v[130:133], v[182:185], v[44:47]
	v_mfma_f32_16x16x32_bf16 v[40:43], v[138:141], v[182:185], v[40:43]
	v_mfma_f32_16x16x32_bf16 v[28:31], v[130:133], v[190:193], v[28:31]
	v_mfma_f32_16x16x32_bf16 v[24:27], v[138:141], v[190:193], v[24:27]
	v_mfma_f32_16x16x32_bf16 v[12:15], v[130:133], v[198:201], v[12:15]
	v_mfma_f32_16x16x32_bf16 v[8:11], v[138:141], v[198:201], v[8:11]
	v_mfma_f32_16x16x32_bf16 v[60:63], v[134:137], v[174:177], v[60:63]
	v_mfma_f32_16x16x32_bf16 v[56:59], v[142:145], v[174:177], v[56:59]
	v_mfma_f32_16x16x32_bf16 v[44:47], v[134:137], v[186:189], v[44:47]
	v_mfma_f32_16x16x32_bf16 v[40:43], v[142:145], v[186:189], v[40:43]
	v_mfma_f32_16x16x32_bf16 v[28:31], v[134:137], v[194:197], v[28:31]
	v_mfma_f32_16x16x32_bf16 v[24:27], v[142:145], v[194:197], v[24:27]
	v_mfma_f32_16x16x32_bf16 v[12:15], v[134:137], v[206:209], v[12:15]
	v_mfma_f32_16x16x32_bf16 v[8:11], v[142:145], v[206:209], v[8:11]
	s_setprio 0
	s_barrier
	s_add_u32 s4, s4, 0x80080
	s_addc_u32 s5, s5, 0
	s_add_i32 s54, s54, s8
	v_lshl_add_u64 v[130:131], s[4:5], 0, v[96:97]
	s_mov_b32 m0, s54
	s_nop 0
	global_load_lds_dwordx4 v[130:131], off
	v_lshl_add_u64 v[130:131], s[4:5], 0, v[146:147]
	s_add_i32 m0, s54, 0x2000
	s_nop 0
	global_load_lds_dwordx4 v[130:131], off
	s_waitcnt vmcnt(6)
	s_barrier
	s_setprio 1
	v_mfma_f32_16x16x32_bf16 v[52:55], v[228:231], v[156:159], v[52:55]
	v_mfma_f32_16x16x32_bf16 v[48:51], v[236:239], v[156:159], v[48:51]
	v_mfma_f32_16x16x32_bf16 v[36:39], v[228:231], v[182:185], v[36:39]
	v_mfma_f32_16x16x32_bf16 v[32:35], v[236:239], v[182:185], v[32:35]
	v_mfma_f32_16x16x32_bf16 v[20:23], v[228:231], v[190:193], v[20:23]
	v_mfma_f32_16x16x32_bf16 v[16:19], v[236:239], v[190:193], v[16:19]
	v_mfma_f32_16x16x32_bf16 v[4:7], v[228:231], v[198:201], v[4:7]
	v_mfma_f32_16x16x32_bf16 v[0:3], v[236:239], v[198:201], v[0:3]
	v_mfma_f32_16x16x32_bf16 v[52:55], v[232:235], v[174:177], v[52:55]
	v_mfma_f32_16x16x32_bf16 v[48:51], v[240:243], v[174:177], v[48:51]
	v_mfma_f32_16x16x32_bf16 v[36:39], v[232:235], v[186:189], v[36:39]
	v_mfma_f32_16x16x32_bf16 v[32:35], v[240:243], v[186:189], v[32:35]
	v_mfma_f32_16x16x32_bf16 v[20:23], v[232:235], v[194:197], v[20:23]
	v_mfma_f32_16x16x32_bf16 v[16:19], v[240:243], v[194:197], v[16:19]
	v_mfma_f32_16x16x32_bf16 v[4:7], v[232:235], v[206:209], v[4:7]
	v_mfma_f32_16x16x32_bf16 v[0:3], v[240:243], v[206:209], v[0:3]
	s_setprio 0
	s_add_i32 s92, s92, 2
	s_add_u32 s36, s36, 0x100
	s_addc_u32 s37, s37, 0
	s_add_u32 s10, s10, 0x100
	s_addc_u32 s24, s24, 0
	s_cmp_gt_u32 s92, 29
	s_barrier
	s_cbranch_scc0 .LBB0_1039
	s_lshl_b32 s4, s88, 8
	s_add_i32 s4, s4, s78
	v_or_b32_e32 v158, s4, v178
	s_ashr_i32 s4, s4, 13
	s_mul_hi_i32 s5, s4, 0x34000
	s_mul_i32 s4, s4, 0x34000
	v_lshl_or_b32 v156, s84, 8, v180
	s_add_u32 s4, s42, s4
	v_ashrrev_i32_e32 v157, 31, v156
	s_addc_u32 s5, s43, s5
	v_lshl_add_u64 v[160:161], v[156:157], 2, s[4:5]
	global_load_dwordx4 v[130:133], v[160:161], off offset:16
	global_load_dwordx4 v[134:137], v[160:161], off
	s_and_b64 vcc, exec, s[44:45]
	s_cbranch_vccnz .Lgpf_skip
	v_lshlrev_b32_e32 v228, 12, v158
	v_lshl_add_u32 v228, v156, 1, v228
	global_load_dword v237, v228, s[40:41]
	global_load_dword v237, v228, s[40:41] offset:256
	v_add_u32_e32 v230, 0x10000, v228
	global_load_dword v237, v230, s[40:41]
	global_load_dword v237, v230, s[40:41] offset:256
	v_add_u32_e32 v231, 0x20000, v228
	global_load_dword v237, v231, s[40:41]
	global_load_dword v237, v231, s[40:41] offset:256
	v_add_u32_e32 v232, 0x30000, v228
	global_load_dword v237, v232, s[40:41]
	global_load_dword v237, v232, s[40:41] offset:256
	v_add_u32_e32 v233, 0x80000, v228
	global_load_dword v237, v233, s[40:41]
	global_load_dword v237, v233, s[40:41] offset:256
	v_add_u32_e32 v234, 0x90000, v228
	global_load_dword v237, v234, s[40:41]
	global_load_dword v237, v234, s[40:41] offset:256
	v_add_u32_e32 v235, 0xa0000, v228
	global_load_dword v237, v235, s[40:41]
	global_load_dword v237, v235, s[40:41] offset:256
	v_add_u32_e32 v236, 0xb0000, v228
	global_load_dword v237, v236, s[40:41]
	global_load_dword v237, v236, s[40:41] offset:256
.Lgpf_skip:
	v_ashrrev_i32_e32 v159, 31, v158
	v_lshlrev_b64 v[138:139], 11, v[158:159]
	v_cndmask_b32_e64 v140, 0, 1, s[44:45]
	v_cmp_ne_u32_e64 s[36:37], 1, v140
	s_andn2_b64 vcc, exec, s[44:45]
	v_lshl_add_u64 v[176:177], v[138:139], 2, s[28:29]
	s_cbranch_vccnz .LBB0_1042
	v_lshl_add_u64 v[142:143], v[156:157], 2, v[176:177]
	global_load_dwordx4 v[138:141], v[142:143], off offset:16
	s_nop 0
	global_load_dwordx4 v[142:145], v[142:143], off
	s_mov_b64 s[4:5], 0
	s_branch .LBB0_1043
